# speedup vs baseline: 1.0315x; 1.0054x over previous
.LBB1_93:
	s_or_b64 exec, exec, s[0:1]
	v_or_b32_e32 v100, s75, v103
	s_add_i32 s18, 0, 0x10000
	v_lshl_add_u32 v100, v100, 4, s18
	v_cmp_lt_i32_e32 vcc, 31, v179
	s_nop 0
	ds_write_b128 v100, v[104:107] offset:512
	s_waitcnt lgkmcnt(0)
	s_barrier
	s_and_saveexec_b64 s[0:1], vcc
	s_xor_b64 s[0:1], exec, s[0:1]
	s_cbranch_execz .LBB1_97
	s_movk_i32 s4, 0xff
	v_cmp_lt_u32_e32 vcc, s4, v179
	s_and_saveexec_b64 s[4:5], vcc
	s_cbranch_execz .LBB1_96
	v_add_u32_e32 v98, 0xffffff00, v179
	v_lshl_add_u32 v101, v98, 2, 0
	v_add_u32_e32 v101, 0x10200, v101
	ds_read2st64_b32 v[110:111], v101 offset1:4
	ds_read2st64_b32 v[112:113], v101 offset0:8 offset1:12
	ds_read2st64_b32 v[114:115], v101 offset0:16 offset1:20
	ds_read2st64_b32 v[116:117], v101 offset0:24 offset1:28
	v_readlane_b32 s19, v240, 3
	v_lshrrev_b32_e32 v98, 4, v98
	v_and_b32_e32 v98, 0xffffffc, v98
	s_waitcnt lgkmcnt(3)
	v_add_f32_e32 v100, 0, v110
	v_add_f32_e32 v100, v100, v111
	s_waitcnt lgkmcnt(2)
	v_add_f32_e32 v100, v100, v112
	v_add_f32_e32 v100, v100, v113
	s_waitcnt lgkmcnt(1)
	v_add_f32_e32 v100, v100, v114
	v_add_f32_e32 v100, v100, v115
	s_waitcnt lgkmcnt(0)
	v_add_f32_e32 v100, v100, v116
	v_add_f32_e32 v100, v100, v117
	v_lshrrev_b32_e32 v101, 2, v179
	v_and_or_b32 v101, v101, 15, s19
	v_readlane_b32 s19, v240, 6
	v_lshlrev_b32_e32 v101, 10, v101
	s_nop 0
	v_and_or_b32 v103, v179, 3, s19
	v_add3_u32 v98, v103, v98, v101
	v_lshl_add_u64 v[104:105], v[98:99], 3, s[52:53]
	v_mov_b32_e32 v101, s27
	global_store_dwordx2 v[104:105], v[100:101], off sc1
